# gcn1/gcn2 CSR staging: both entries of a thread loaded in one round trip (was a serialized 2-iteration loop)
# baseline (speedup 1.0000x reference)
.LBB4_2:
	s_or_b64 exec, exec, s[8:9]
	s_movk_i32 s8, 0x5400
	v_mov_b32_e32 v2, 0
	v_add_u32_e64 v3, s8, 0
	s_load_dwordx2 s[12:13], s[0:1], 0x68
	s_load_dwordx2 s[16:17], s[0:1], 0x58
	s_waitcnt lgkmcnt(0)
	s_barrier
	ds_read2_b32 v[18:19], v3 offset0:64 offset1:127
	ds_read_b32 v2, v2 offset:22268
	s_load_dwordx2 s[20:21], s[0:1], 0x0
	s_load_dwordx4 s[8:11], s[0:1], 0x30
	s_waitcnt lgkmcnt(0)
	v_sub_u32_e32 v3, v19, v18
	v_add_u32_e32 v8, v3, v2
	v_cmp_lt_i32_e32 vcc, v0, v8
	s_and_saveexec_b64 s[14:15], vcc
	s_cbranch_execz .LBB4_7
	s_load_dwordx2 s[18:19], s[0:1], 0x10
	v_add_u32_e32 v4, v0, v18
	v_mov_b32_e32 v2, 0x4400
	v_lshl_add_u32 v9, v0, 3, v2
	v_lshlrev_b32_e32 v2, 3, v4
	v_lshlrev_b32_e32 v4, 2, v4
	v_mov_b32_e32 v10, v0
	s_movk_i32 s28, 0x200
	s_mov_b64 s[22:23], 0
	s_waitcnt lgkmcnt(0)
.Lg1s_loop:
	global_load_dwordx2 v[6:7], v2, s[4:5]
	v_add_u32_e32 v3, 0x100, v10
	v_cmp_lt_i32_e32 vcc, v3, v8
	s_and_saveexec_b64 s[26:27], vcc
	global_load_dwordx2 v[12:13], v2, s[4:5] offset:2048
	s_mov_b64 exec, s[26:27]
	s_waitcnt vmcnt(0)
	v_lshlrev_b32_e32 v5, 2, v6
	global_load_dword v11, v5, s[6:7]
	s_and_saveexec_b64 s[26:27], vcc
	v_lshlrev_b32_e32 v5, 2, v12
	global_load_dword v14, v5, s[6:7]
	s_mov_b64 exec, s[26:27]
	s_waitcnt vmcnt(0)
	v_mul_f32_e32 v7, v7, v11
	global_store_dword v4, v7, s[18:19]
	v_cmp_gt_u32_e64 s[24:25], s28, v10
	s_and_saveexec_b64 s[26:27], s[24:25]
	ds_write_b64 v9, v[6:7]
	s_mov_b64 exec, s[26:27]
	s_and_saveexec_b64 s[26:27], vcc
	v_mul_f32_e32 v13, v13, v14
	global_store_dword v4, v13, s[18:19] offset:1024
	v_cmp_gt_u32_e64 s[24:25], s28, v3
	s_and_b64 exec, exec, s[24:25]
	ds_write_b64 v9, v[12:13] offset:2048
	s_mov_b64 exec, s[26:27]
	v_add_u32_e32 v10, 0x200, v10
	v_cmp_ge_i32_e32 vcc, v10, v8
	v_add_u32_e32 v9, 0x1000, v9
	v_add_u32_e32 v2, 0x1000, v2
	v_add_u32_e32 v4, 0x800, v4
	s_or_b64 s[22:23], vcc, s[22:23]
	s_andn2_b64 exec, exec, s[22:23]
	s_cbranch_execnz .Lg1s_loop

.LBB5_4:
	s_or_b64 exec, exec, s[8:9]
	s_movk_i32 s4, 0x5800
	v_mov_b32_e32 v1, 0
	v_add_u32_e64 v2, s4, 0
	s_waitcnt lgkmcnt(0)
	s_barrier
	ds_read2_b32 v[82:83], v2 offset0:64 offset1:127
	ds_read_b32 v1, v1 offset:23292
	s_load_dwordx8 s[8:15], s[0:1], 0x68
	s_load_dwordx2 s[26:27], s[0:1], 0x0
	s_load_dwordx4 s[16:19], s[0:1], 0x30
	s_waitcnt lgkmcnt(0)
	v_sub_u32_e32 v2, v83, v82
	v_add_u32_e32 v1, v2, v1
	v_cmp_lt_i32_e32 vcc, v78, v1
	s_and_saveexec_b64 s[4:5], vcc
	s_cbranch_execz .LBB5_9
	v_add_u32_e32 v4, v82, v78
	v_mov_b32_e32 v2, 0x4400
	v_lshl_add_u32 v2, v78, 3, v2
	v_lshlrev_b32_e32 v5, 2, v4
	v_lshlrev_b32_e32 v4, 3, v4
	global_load_dword v7, v5, s[22:23]
	global_load_dword v6, v4, s[20:21]
	v_add_u32_e32 v3, 0x100, v78
	v_cmp_lt_i32_e32 vcc, v3, v1
	s_and_saveexec_b64 s[24:25], vcc
	global_load_dword v9, v5, s[22:23] offset:1024
	global_load_dword v8, v4, s[20:21] offset:2048
	s_mov_b64 exec, s[24:25]
	s_waitcnt vmcnt(0)
	ds_write_b64 v2, v[6:7]
	s_and_b64 exec, exec, vcc
	ds_write_b64 v2, v[8:9] offset:2048
